# attention unit loop: the once-per-phase first-key-tile word is waited for before the loop instead of vmcnt(0) at every unit (which drained the previous unit's stores); + dummy-store wait removal, down
# baseline (speedup 1.0000x reference)
.LBB0_2089:
	s_or_b64 exec, exec, s[8:9]
	s_waitcnt lgkmcnt(0)
	s_barrier
	s_load_dwordx2 s[0:1], s[90:91], 0xc8
	s_waitcnt vmcnt(1)
	v_lshrrev_b32_e32 v2, 1, v0
	v_and_b32_e32 v2, 6, v2
	v_and_b32_e32 v1, 3, v0
	v_lshlrev_b32_e32 v3, 3, v0
	s_waitcnt lgkmcnt(0)
	s_add_u32 s40, s0, 0x2ec00000
	s_addc_u32 s41, s1, 0
	s_add_u32 s42, s0, 0x36c00000
	s_addc_u32 s43, s1, 0
	s_add_u32 s44, s0, 0x3ec00000
	s_addc_u32 s45, s1, 0
	s_add_u32 s46, s0, 0x4fc00000
	s_addc_u32 s47, s1, 0
	s_add_u32 s48, s0, 0x1800000
	s_addc_u32 s49, s1, 0
	s_lshr_b32 s3, s57, 29
	s_add_i32 s3, s97, s3
	s_ashr_i32 s3, s3, 3
	s_mul_i32 s50, s3, s64
	v_readlane_b32 s3, v254, 12
	s_add_i32 s50, s50, s3
	v_add_u32_e32 v2, s50, v2
	v_and_b32_e32 v2, 7, v2
	v_mul_u32_u24_e32 v5, 3, v2
	v_add3_u32 v5, v5, v1, 4
	v_cmp_eq_u32_e32 vcc, 0, v1
	s_ashr_i32 s51, s50, 3
	v_and_b32_e32 v3, 0x60, v3
	v_lshl_or_b32 v4, v2, 2, v1
	v_cndmask_b32_e32 v1, v5, v2, vcc
	v_cmp_gt_u32_e32 vcc, 5, v2
	v_add_u32_e32 v3, s51, v3
	s_movk_i32 s22, 0xe000
	v_cndmask_b32_e32 v1, v4, v1, vcc
	v_lshl_add_u32 v2, v3, 5, v1
	v_ashrrev_i32_e32 v3, 31, v2
	v_lshl_add_u64 v[2:3], v[2:3], 2, s[0:1]
	s_mov_b32 s0, 0x420000
	v_add_co_u32_e32 v2, vcc, s0, v2
	s_mov_b32 s13, 0
	s_nop 0
	v_addc_co_u32_e32 v3, vcc, 0, v3, vcc
	global_load_dword v1, v[2:3], off
	v_mov_b32_e32 v3, 0
	s_mov_b64 s[14:15], 0x2000
	s_mov_b64 s[16:17], 0x4000
	s_add_i32 s69, 0, 0x14800
	s_movk_i32 s72, 0xc0
	s_mov_b64 s[18:19], 0x6000
	s_mov_b64 s[20:21], 0xa000
	s_add_i32 s73, 0, 0x14900
	s_mov_b32 s23, -1
	s_mov_b64 s[24:25], 0x8000
	s_mov_b32 s74, 0x42700000
	v_mov_b32_e32 v194, 0xff800000
	s_mov_b32 s75, 0
	s_waitcnt vmcnt(0)
	s_branch .LBB0_2093

.LBB0_2100:
	s_ashr_i32 s1, s77, 31
	s_lshr_b32 s1, s1, 28
	s_add_i32 s1, s77, s1
	s_nop 0
	v_readlane_b32 s10, v1, s75
	s_ashr_i32 s26, s1, 4
	s_and_b32 s1, s1, -16
	s_and_b32 s0, s10, 0x10000
	s_sub_i32 s1, s77, s1
	s_cmp_eq_u32 s0, 0
	s_cbranch_scc1 .LBB0_2152
	v_mov_b32_e32 v38, v0
	s_ashr_i32 s27, s26, 31
	v_readfirstlane_b32 s3, v38
	s_lshl_b32 s30, s76, 8
	s_and_b32 s33, s10, 0xffff
	s_ashr_i32 s0, s3, 6
	s_lshl_b64 s[4:5], s[26:27], 13
	s_ashr_i32 s31, s30, 31
	s_add_u32 s4, s4, s30
	s_addc_u32 s5, s5, s31
	s_lshl_b32 s11, s0, 5
	s_ashr_i32 s6, s11, 31
	s_add_u32 s8, s4, s11
	s_addc_u32 s9, s5, s6
	s_lshl_b64 s[4:5], s[8:9], 11
	s_add_u32 s6, s40, s4
	s_addc_u32 s7, s41, s5
	s_lshl_b32 s28, s1, 6
	s_ashr_i32 s29, s28, 31
	s_lshl_b64 s[4:5], s[28:29], 1
	s_add_u32 s36, s6, s4
	s_addc_u32 s37, s7, s5
	s_lshl_b32 s4, s26, 4
	s_add_i32 s34, s4, s1
	s_ashr_i32 s35, s34, 31
	s_lshl_b64 s[4:5], s[34:35], 19
	s_lshl_b32 s6, s33, 12
	s_add_u32 s4, s4, s6
	s_addc_u32 s5, s5, 0
	s_lshl_b64 s[4:5], s[4:5], 1
	s_add_u32 s12, s42, s4
	s_addc_u32 s27, s43, s5
	s_lshl_b32 s6, s0, 9
	s_ashr_i32 s7, s6, 31
	s_lshl_b64 s[6:7], s[6:7], 1
	v_and_b32_e32 v195, 63, v38
	s_add_u32 s6, s12, s6
	s_addc_u32 s7, s27, s7
	v_lshlrev_b32_e32 v2, 4, v195
	v_lshl_add_u64 v[180:181], s[6:7], 0, v[2:3]
	s_add_u32 s6, s44, s4
	s_addc_u32 s7, s45, s5
	s_lshl_b32 s4, s3, 3
	s_and_b32 s4, s4, 0xfffff800
	s_ashr_i32 s5, s4, 31
	s_lshl_b64 s[4:5], s[4:5], 1
	s_add_u32 s4, s6, s4
	s_addc_u32 s5, s7, s5
	s_lshl_b32 s7, s0, 10
	s_and_b32 s6, s7, 0xc00
	s_add_u32 s4, s4, s6
	s_addc_u32 s5, s5, 0
	s_cmp_lg_u32 0, -1
	v_lshl_add_u64 v[36:37], s[4:5], 0, v[2:3]
	s_cselect_b32 s4, 0, 0
	v_and_b32_e32 v196, 31, v38
	s_add_i32 s5, s7, s4
	s_mov_b32 s4, m0
	s_mov_b32 m0, s5
	s_nop 0
	global_load_lds_dwordx4 v[180:181], off
	s_mov_b32 m0, s4
	v_bfe_u32 v39, v38, 5, 1
	s_add_i32 s6, s5, 0x6000
	s_mov_b32 s4, m0
	s_mov_b32 m0, s6
	s_nop 0
	global_load_lds_dwordx4 v[36:37], off
	s_mov_b32 m0, s4
	v_lshlrev_b32_e32 v2, 11, v196
	v_lshl_add_u64 v[4:5], v[180:181], 0, s[14:15]
	s_add_i32 s4, s5, 0x2000
	s_mov_b32 s12, m0
	s_mov_b32 m0, s4
	s_nop 0
	global_load_lds_dwordx4 v[4:5], off
	s_mov_b32 m0, s12
	v_lshl_or_b32 v2, v39, 4, v2
	global_load_dwordx4 v[128:131], v2, s[36:37]
	global_load_dwordx4 v[124:127], v2, s[36:37] offset:32
	global_load_dwordx4 v[120:123], v2, s[36:37] offset:64
	global_load_dwordx4 v[116:119], v2, s[36:37] offset:96
	s_add_i32 s4, s30, 0x100
	s_ashr_i32 s27, s4, 6
	s_sub_i32 s4, s27, s33
	v_lshl_add_u64 v[4:5], v[180:181], 0, s[16:17]
	s_add_i32 s12, s5, 0x4000
	s_mov_b32 s36, m0
	s_mov_b32 m0, s12
	s_nop 0
	global_load_lds_dwordx4 v[4:5], off
	s_mov_b32 m0, s36
	s_lshl_b32 s12, s4, 6
	v_lshlrev_b32_e32 v4, 2, v38
	v_lshlrev_b32_e32 v40, 4, v38
	v_cmp_gt_i32_e32 vcc, s12, v4
	s_and_saveexec_b64 s[36:37], vcc
	s_cbranch_execz .LBB0_2104
	s_lshl_b64 s[34:35], s[34:35], 15
	s_add_u32 s38, s48, s34
	s_addc_u32 s39, s49, s35
	s_lshl_b64 s[30:31], s[30:31], 2
	s_add_u32 s30, s38, s30
	s_addc_u32 s31, s39, s31
	global_load_dword v2, v3, s[30:31] offset:1020
	s_lshl_b32 s30, s33, 8
	s_add_u32 s30, s34, s30
	s_addc_u32 s31, s35, 0
	s_add_u32 s30, s48, s30
	v_ashrrev_i32_e32 v5, 31, v4
	s_addc_u32 s31, s49, s31
	v_add_u32_e32 v8, s69, v40
	v_lshl_add_u64 v[6:7], v[4:5], 2, s[30:31]
	s_mov_b64 s[30:31], 0
